# baseline K1; hand-written agg (two columns per wave in half-waves); final_kernel: H2 loads and kernarg loads issued before the BN-stats barrier; agg2: stats pointers loaded with the first kernargs
# speedup vs baseline: 1.0117x; 1.0117x over previous
_Z11agg2_kernelPKiPKfPK15HIP_vector_typeIiLj2EEPKDF16_S2_S2_S2_S2_S2_PfS9_:
	s_load_dwordx8 s[12:19], s[0:1], 0x0
	s_load_dwordx2 s[4:5], s[0:1], 0x38
	s_load_dwordx4 s[36:39], s[0:1], 0x20
	s_load_dwordx2 s[40:41], s[0:1], 0x30
	v_lshrrev_b32_e32 v1, 6, v0
	s_lshl_b32 s3, s2, 4
	v_lshlrev_b32_e32 v63, 1, v1
	v_or_b32_e32 v34, s3, v63
	v_lshlrev_b32_e32 v7, 4, v0
	v_ashrrev_i32_e32 v35, 31, v34
	v_mov_b32_e32 v19, 0
	v_and_b32_e32 v18, 0xf0, v7
	v_lshrrev_b32_e32 v7, 4, v0
	v_or_b32_e32 v8, 0x200, v0
	v_lshlrev_b64 v[4:5], 2, v[34:35]
	s_waitcnt lgkmcnt(0)
	v_lshl_add_u64 v[16:17], s[4:5], 0, v[18:19]
	v_lshlrev_b32_e32 v20, 8, v7
	v_mov_b32_e32 v21, v19
	v_lshrrev_b32_e32 v30, 4, v8
	v_lshl_add_u64 v[2:3], s[12:13], 0, v[4:5]
	v_lshl_add_u64 v[4:5], s[14:15], 0, v[4:5]
	v_lshl_add_u64 v[22:23], v[16:17], 0, v[20:21]
	v_lshlrev_b32_e32 v8, 8, v30
	v_mov_b32_e32 v9, v19
	global_load_dword v35, v[2:3], off
	global_load_dword v6, v[4:5], off
	v_lshl_add_u64 v[24:25], v[16:17], 0, v[8:9]
	global_load_dwordx4 v[8:11], v[22:23], off
	global_load_dwordx4 v[12:15], v[24:25], off
	v_or_b32_e32 v20, 0x4000, v20
	v_lshl_add_u64 v[28:29], v[16:17], 0, v[20:21]
	v_or_b32_e32 v20, 0x600, v0
	v_bfe_u32 v61, v0, 4, 2
	v_lshlrev_b32_e32 v57, 6, v34
	v_lshrrev_b32_e32 v31, 4, v20
	v_or_b32_e32 v50, v57, v61
	v_mov_b32_e32 v51, v19
	v_lshlrev_b32_e32 v20, 8, v31
	v_lshl_add_u64 v[54:55], v[50:51], 3, s[16:17]
	v_lshl_add_u64 v[16:17], v[16:17], 0, v[20:21]
	global_load_dwordx4 v[20:23], v[28:29], off
	global_load_dwordx4 v[24:27], v[16:17], off
	global_load_dwordx2 v[44:45], v[54:55], off
	global_load_dwordx2 v[46:47], v[54:55], off offset:32
	global_load_dwordx2 v[48:49], v[54:55], off offset:64
	global_load_dwordx2 v[52:53], v[54:55], off offset:96
	s_movk_i32 s4, 0x110
	s_movk_i32 s5, 0x80
	v_mad_u32_u24 v7, v7, s4, v18
	v_cmp_gt_u32_e32 vcc, s5, v0
	v_mad_u32_u24 v16, v30, s4, v18
	v_mad_u32_u24 v17, v31, s4, v18
	s_waitcnt vmcnt(7)
	ds_write_b128 v7, v[8:11]
	s_waitcnt vmcnt(6)
	ds_write_b128 v16, v[12:15]
	s_waitcnt vmcnt(5)
	ds_write_b128 v7, v[20:23] offset:17408
	s_waitcnt vmcnt(4)
	ds_write_b128 v17, v[24:27]
	s_and_saveexec_b64 s[8:9], vcc
	s_cbranch_execz .LBB1_2
	v_lshlrev_b32_e32 v18, 2, v0
	s_movk_i32 s12, 0x1000
	global_load_dword v7, v18, s[36:37]
	global_load_dword v10, v18, s[36:37] offset:512
	global_load_dword v12, v18, s[36:37] offset:1024
	global_load_dword v14, v18, s[36:37] offset:1536
	global_load_dword v16, v18, s[36:37] offset:2048
	global_load_dword v20, v18, s[36:37] offset:2560
	global_load_dword v22, v18, s[36:37] offset:3072
	global_load_dword v24, v18, s[36:37] offset:3584
	v_lshl_add_u64 v[8:9], s[36:37], 0, v[18:19]
	v_add_co_u32_e32 v8, vcc, s12, v8
	s_mov_b32 s4, 0x55555555
	s_nop 0
	v_addc_co_u32_e32 v9, vcc, 0, v9, vcc
	global_load_dword v26, v[8:9], off
	global_load_dword v27, v[8:9], off offset:512
	global_load_dword v28, v[8:9], off offset:1024
	global_load_dword v29, v[8:9], off offset:1536
	global_load_dword v30, v[8:9], off offset:2048
	global_load_dword v32, v[8:9], off offset:2560
	global_load_dword v36, v[8:9], off offset:3072
	global_load_dword v38, v[8:9], off offset:3584
	global_load_dword v40, v18, s[38:39]
	global_load_dword v41, v18, s[40:41]
	s_mov_b32 s5, 0x3f155555
	s_mov_b32 s6, 0x800000
	s_waitcnt vmcnt(17)
	v_cvt_f64_f32_e32 v[8:9], v7
	v_add_f64 v[8:9], v[8:9], 0
	s_waitcnt vmcnt(15)
	v_cvt_f64_f32_e32 v[12:13], v12
	v_cvt_f64_f32_e32 v[10:11], v10
	s_waitcnt vmcnt(13)
	v_cvt_f64_f32_e32 v[16:17], v16
	v_add_f64 v[8:9], v[8:9], v[12:13]
	v_cvt_f64_f32_e32 v[14:15], v14
	s_waitcnt vmcnt(11)
	v_cvt_f64_f32_e32 v[22:23], v22
	v_add_f64 v[10:11], v[10:11], 0
	v_add_f64 v[8:9], v[8:9], v[16:17]
	v_cvt_f64_f32_e32 v[20:21], v20
	v_add_f64 v[10:11], v[10:11], v[14:15]
	s_waitcnt vmcnt(9)
	v_cvt_f64_f32_e32 v[12:13], v26
	v_add_f64 v[8:9], v[8:9], v[22:23]
	v_cvt_f64_f32_e32 v[24:25], v24
	s_waitcnt vmcnt(8)
	v_cvt_f64_f32_e32 v[14:15], v27
	s_waitcnt vmcnt(7)
	v_cvt_f64_f32_e32 v[26:27], v28
	v_add_f64 v[10:11], v[10:11], v[20:21]
	v_add_f64 v[8:9], v[8:9], v[12:13]
	s_waitcnt vmcnt(5)
	v_cvt_f64_f32_e32 v[30:31], v30
	v_add_f64 v[10:11], v[10:11], v[24:25]
	v_add_f64 v[8:9], v[8:9], v[26:27]
	v_cvt_f64_f32_e32 v[28:29], v29
	s_waitcnt vmcnt(3)
	v_cvt_f64_f32_e32 v[36:37], v36
	v_add_f64 v[10:11], v[10:11], v[14:15]
	v_add_f64 v[8:9], v[8:9], v[30:31]
	v_cvt_f64_f32_e32 v[32:33], v32
	v_add_f64 v[10:11], v[10:11], v[28:29]
	v_add_f64 v[8:9], v[8:9], v[36:37]
	s_waitcnt vmcnt(2)
	v_cvt_f64_f32_e32 v[38:39], v38
	v_add_f64 v[10:11], v[10:11], v[32:33]
	v_mul_f64 v[8:9], v[8:9], s[4:5]
	v_add_f64 v[10:11], v[10:11], v[38:39]
	v_mul_f64 v[12:13], v[8:9], v[8:9]
	v_fma_f64 v[10:11], v[10:11], s[4:5], -v[12:13]
	v_cmp_ngt_f64_e32 vcc, 0, v[10:11]
	v_cvt_f32_f64_e32 v8, v[8:9]
	s_nop 0
	v_cndmask_b32_e32 v11, 0, v11, vcc
	v_cndmask_b32_e32 v10, 0, v10, vcc
	v_cvt_f32_f64_e32 v7, v[10:11]
	v_add_f32_e32 v7, 0x3727c5ac, v7
	v_mul_f32_e32 v10, 0x4b800000, v7
	v_cmp_gt_f32_e32 vcc, s6, v7
	s_nop 1
	v_cndmask_b32_e32 v7, v7, v10, vcc
	v_rsq_f32_e32 v7, v7
	s_nop 0
	v_mul_f32_e32 v9, 0x45800000, v7
	v_cndmask_b32_e32 v7, v7, v9, vcc
	s_waitcnt vmcnt(1)
	v_mul_f32_e32 v7, v7, v40
	s_waitcnt vmcnt(0)
	v_fma_f32 v8, -v8, v7, v41
	v_add_u32_e32 v9, 0x80, v18
	ds_write2st64_b32 v9, v7, v8 offset0:168 offset1:170

_Z12final_kernelPKfS0_S0_S0_Pf:
	s_load_dwordx2 s[12:13], s[0:1], 0x0
	s_load_dwordx4 s[4:7], s[0:1], 0x8
	s_load_dwordx2 s[10:11], s[0:1], 0x18
	s_load_dwordx2 s[14:15], s[0:1], 0x20
	v_lshl_or_b32 v36, s2, 8, v0
	v_lshlrev_b32_e32 v37, 4, v36
	v_add_u32_e32 v38, 0x200000, v37
	v_lshlrev_b32_e32 v1, 2, v0
	s_waitcnt lgkmcnt(0)
	global_load_dwordx4 v[40:43], v37, s[12:13]
	s_cmp_lt_u32 s2, 0x100
	s_cbranch_scc0 .Lfin_one
	global_load_dwordx4 v[44:47], v38, s[12:13]
.Lfin_one:
	v_cmp_gt_u32_e32 vcc, 64, v0
	s_and_saveexec_b64 s[8:9], vcc
	s_cbranch_execz .Lfin_nostat
	s_mov_b32 s3, 0x800000
	global_load_dword v2, v1, s[4:5]
	global_load_dword v4, v1, s[4:5] offset:256
	global_load_dword v6, v1, s[4:5] offset:512
	global_load_dword v8, v1, s[4:5] offset:768
	global_load_dword v10, v1, s[4:5] offset:1024
	global_load_dword v12, v1, s[4:5] offset:1280
	global_load_dword v14, v1, s[4:5] offset:1536
	global_load_dword v16, v1, s[4:5] offset:1792
	global_load_dword v18, v1, s[4:5] offset:2048
	global_load_dword v20, v1, s[4:5] offset:2304
	global_load_dword v22, v1, s[4:5] offset:2560
	global_load_dword v24, v1, s[4:5] offset:2816
	global_load_dword v26, v1, s[4:5] offset:3072
	global_load_dword v28, v1, s[4:5] offset:3328
	global_load_dword v30, v1, s[4:5] offset:3584
	global_load_dword v32, v1, s[4:5] offset:3840
	global_load_dword v34, v1, s[6:7]
	global_load_dword v35, v1, s[10:11]
	s_mov_b32 s4, 0x55555555
	s_mov_b32 s5, 0x3f155555
	s_waitcnt vmcnt(17)
	v_cvt_f64_f32_e32 v[2:3], v2
	v_add_f64 v[2:3], v[2:3], 0
	s_waitcnt vmcnt(15)
	v_cvt_f64_f32_e32 v[6:7], v6
	v_cvt_f64_f32_e32 v[4:5], v4
	s_waitcnt vmcnt(13)
	v_cvt_f64_f32_e32 v[10:11], v10
	v_add_f64 v[2:3], v[2:3], v[6:7]
	v_cvt_f64_f32_e32 v[8:9], v8
	s_waitcnt vmcnt(11)
	v_cvt_f64_f32_e32 v[14:15], v14
	v_add_f64 v[4:5], v[4:5], 0
	v_add_f64 v[2:3], v[2:3], v[10:11]
	v_cvt_f64_f32_e32 v[12:13], v12
	s_waitcnt vmcnt(9)
	v_cvt_f64_f32_e32 v[18:19], v18
	v_add_f64 v[4:5], v[4:5], v[8:9]
	v_add_f64 v[2:3], v[2:3], v[14:15]
	v_cvt_f64_f32_e32 v[16:17], v16
	s_waitcnt vmcnt(7)
	v_cvt_f64_f32_e32 v[22:23], v22
	v_add_f64 v[4:5], v[4:5], v[12:13]
	v_add_f64 v[2:3], v[2:3], v[18:19]
	v_cvt_f64_f32_e32 v[20:21], v20
	s_waitcnt vmcnt(5)
	v_cvt_f64_f32_e32 v[26:27], v26
	v_add_f64 v[4:5], v[4:5], v[16:17]
	v_add_f64 v[2:3], v[2:3], v[22:23]
	v_cvt_f64_f32_e32 v[24:25], v24
	s_waitcnt vmcnt(3)
	v_cvt_f64_f32_e32 v[30:31], v30
	v_add_f64 v[4:5], v[4:5], v[20:21]
	v_add_f64 v[2:3], v[2:3], v[26:27]
	v_cvt_f64_f32_e32 v[28:29], v28
	v_add_f64 v[4:5], v[4:5], v[24:25]
	v_add_f64 v[2:3], v[2:3], v[30:31]
	s_waitcnt vmcnt(2)
	v_cvt_f64_f32_e32 v[32:33], v32
	v_add_f64 v[4:5], v[4:5], v[28:29]
	v_mul_f64 v[2:3], v[2:3], s[4:5]
	v_add_f64 v[4:5], v[4:5], v[32:33]
	v_mul_f64 v[6:7], v[2:3], v[2:3]
	v_fma_f64 v[4:5], v[4:5], s[4:5], -v[6:7]
	v_cmp_ngt_f64_e32 vcc, 0, v[4:5]
	v_cvt_f32_f64_e32 v2, v[2:3]
	s_nop 0
	v_cndmask_b32_e32 v5, 0, v5, vcc
	v_cndmask_b32_e32 v4, 0, v4, vcc
	v_cvt_f32_f64_e32 v4, v[4:5]
	v_add_f32_e32 v4, 0x3727c5ac, v4
	v_mul_f32_e32 v5, 0x4b800000, v4
	v_cmp_gt_f32_e32 vcc, s3, v4
	s_nop 1
	v_cndmask_b32_e32 v4, v4, v5, vcc
	v_rsq_f32_e32 v4, v4
	s_nop 0
	v_mul_f32_e32 v5, 0x45800000, v4
	v_cndmask_b32_e32 v4, v4, v5, vcc
	s_waitcnt vmcnt(1)
	v_mul_f32_e32 v4, v4, v34
	s_waitcnt vmcnt(0)
	v_fma_f32 v2, -v2, v4, v35
	ds_write2st64_b32 v1, v4, v2 offset1:1
.Lfin_nostat:
	s_or_b64 exec, exec, s[8:9]
	v_and_b32_e32 v48, 15, v0
	v_lshlrev_b32_e32 v48, 4, v48
	s_waitcnt lgkmcnt(0)
	s_barrier
	ds_read_b128 v[8:11], v48
	ds_read_b128 v[12:15], v48 offset:256
	s_waitcnt vmcnt(0) lgkmcnt(0)
	v_pk_fma_f32 v[42:43], v[42:43], v[10:11], v[14:15]
	v_pk_fma_f32 v[40:41], v[40:41], v[8:9], v[12:13]
	global_store_dwordx4 v37, v[40:43], s[14:15]
	s_cmp_lt_u32 s2, 0x100
	s_cbranch_scc0 .Lfin_end
	v_pk_fma_f32 v[46:47], v[46:47], v[10:11], v[14:15]
	v_pk_fma_f32 v[44:45], v[44:45], v[8:9], v[12:13]
	global_store_dwordx4 v38, v[44:47], s[14:15]

	.amdhsa_kernel _Z12final_kernelPKfS0_S0_S0_Pf
		.amdhsa_group_segment_fixed_size 512
		.amdhsa_private_segment_fixed_size 0
		.amdhsa_kernarg_size 296
		.amdhsa_user_sgpr_count 2
		.amdhsa_user_sgpr_dispatch_ptr 0
		.amdhsa_user_sgpr_queue_ptr 0
		.amdhsa_user_sgpr_kernarg_segment_ptr 1
		.amdhsa_user_sgpr_dispatch_id 0
		.amdhsa_user_sgpr_kernarg_preload_length 0
		.amdhsa_user_sgpr_kernarg_preload_offset 0
		.amdhsa_user_sgpr_private_segment_size 0
		.amdhsa_uses_dynamic_stack 0
		.amdhsa_enable_private_segment 0
		.amdhsa_system_sgpr_workgroup_id_x 1
		.amdhsa_system_sgpr_workgroup_id_y 0
		.amdhsa_system_sgpr_workgroup_id_z 0
		.amdhsa_system_sgpr_workgroup_info 0
		.amdhsa_system_vgpr_workitem_id 0
		.amdhsa_next_free_vgpr 49
		.amdhsa_next_free_sgpr 16
		.amdhsa_accum_offset 52
		.amdhsa_reserve_vcc 1
		.amdhsa_float_round_mode_32 0
		.amdhsa_float_round_mode_16_64 0
		.amdhsa_float_denorm_mode_32 3
		.amdhsa_float_denorm_mode_16_64 3
		.amdhsa_dx10_clamp 1
		.amdhsa_ieee_mode 1
		.amdhsa_fp16_overflow 0
		.amdhsa_tg_split 0
		.amdhsa_exception_fp_ieee_invalid_op 0
		.amdhsa_exception_fp_denorm_src 0
		.amdhsa_exception_fp_ieee_div_zero 0
		.amdhsa_exception_fp_ieee_overflow 0
		.amdhsa_exception_fp_ieee_underflow 0
		.amdhsa_exception_fp_ieee_inexact 0
		.amdhsa_exception_int_div_zero 0
	.end_amdhsa_kernel

.Lfunc_end2:
	.size	_Z12final_kernelPKfS0_S0_S0_Pf, .Lfunc_end2-_Z12final_kernelPKfS0_S0_S0_Pf
	.set _Z12final_kernelPKfS0_S0_S0_Pf.num_vgpr, 49
	.set _Z12final_kernelPKfS0_S0_S0_Pf.num_agpr, 0
	.set _Z12final_kernelPKfS0_S0_S0_Pf.numbered_sgpr, 12
	.set _Z12final_kernelPKfS0_S0_S0_Pf.num_named_barrier, 0
	.set _Z12final_kernelPKfS0_S0_S0_Pf.private_seg_size, 0
	.set _Z12final_kernelPKfS0_S0_S0_Pf.uses_vcc, 1
	.set _Z12final_kernelPKfS0_S0_S0_Pf.uses_flat_scratch, 0
	.set _Z12final_kernelPKfS0_S0_S0_Pf.has_dyn_sized_stack, 0
	.set _Z12final_kernelPKfS0_S0_S0_Pf.has_recursion, 0
	.set _Z12final_kernelPKfS0_S0_S0_Pf.has_indirect_call, 0

.Lagg_slow_loop:
	v_cmp_lt_u32_e32 vcc, s20, v7
	s_cbranch_vccz .Lagg_slow_done
	v_add_u32_e32 v35, s20, v34
	v_mul_u32_u24_e32 v36, 0x3000, v1
	v_add3_u32 v36, v36, v35, s34
	v_lshl_add_u32 v37, v1, 6, v35
	v_cmp_gt_u32_e32 vcc, 64, v35
	s_nop 1
	v_cndmask_b32_e32 v36, v36, v37, vcc
	v_lshlrev_b32_e32 v36, 3, v36
	global_load_dwordx2 v[16:17], v36, s[8:9]
	v_cmp_lt_u32_e64 s[40:41], v35, v7
	s_waitcnt vmcnt(0)
	v_cndmask_b32_e64 v16, v1, v16, s[40:41]
	v_cndmask_b32_e64 v17, 0, v17, s[40:41]
	v_lshlrev_b32_e32 v32, 2, v16
	v_lshl_add_u32 v16, v16, 8, v2
	global_load_dword v32, v32, s[6:7]
	global_load_dwordx4 v[40:43], v16, s[12:13]
	s_waitcnt vmcnt(0)
	v_add_f32_e32 v8, 1.0, v32
	v_mul_f32_e32 v10, 0x4b800000, v8
	v_cmp_gt_f32_e32 vcc, s33, v8
	s_nop 1
	v_cndmask_b32_e32 v10, v8, v10, vcc
	v_rsq_f32_e32 v11, v10
	s_nop 0
	v_mul_f32_e32 v10, 0x45800000, v11
	v_cndmask_b32_e32 v11, v11, v10, vcc
	v_cmp_lt_f32_e32 vcc, 0, v8
	s_nop 1
	v_cndmask_b32_e32 v11, 0, v11, vcc
	v_mul_f32_e32 v32, v17, v11
	v_cmp_eq_u32_e32 vcc, 0, v2
	s_and_b64 vcc, vcc, s[40:41]
	s_and_saveexec_b64 s[22:23], vcc
	global_store_dword v36, v32, s[8:9] offset:4
	s_mov_b64 exec, s[22:23]
	v_cvt_f32_f16_sdwa v11, v40 dst_sel:DWORD dst_unused:UNUSED_PAD src0_sel:WORD_1
	v_cvt_f32_f16_e32 v8, v40
	v_fmac_f32_e32 v72, v32, v8
	v_fmac_f32_e32 v73, v32, v11
	v_cvt_f32_f16_sdwa v11, v41 dst_sel:DWORD dst_unused:UNUSED_PAD src0_sel:WORD_1
	v_cvt_f32_f16_e32 v8, v41
	v_fmac_f32_e32 v74, v32, v8
	v_fmac_f32_e32 v75, v32, v11
	v_cvt_f32_f16_sdwa v11, v42 dst_sel:DWORD dst_unused:UNUSED_PAD src0_sel:WORD_1
	v_cvt_f32_f16_e32 v8, v42
	v_fmac_f32_e32 v76, v32, v8
	v_fmac_f32_e32 v77, v32, v11
	v_cvt_f32_f16_sdwa v11, v43 dst_sel:DWORD dst_unused:UNUSED_PAD src0_sel:WORD_1
	v_cvt_f32_f16_e32 v8, v43
	v_fmac_f32_e32 v78, v32, v8
	v_fmac_f32_e32 v79, v32, v11
	s_add_u32 s20, s20, 2
	s_branch .Lagg_slow_loop

amdhsa.kernels:
  - .agpr_count:     0
    .args:
      - .actual_access:  read_only
        .address_space:  global
        .offset:         0
        .size:           8
        .value_kind:     global_buffer
      - .actual_access:  read_only
        .address_space:  global
        .offset:         8
        .size:           8
        .value_kind:     global_buffer
      - .actual_access:  read_only
        .address_space:  global
        .offset:         16
        .size:           8
        .value_kind:     global_buffer
      - .actual_access:  write_only
        .address_space:  global
        .offset:         24
        .size:           8
        .value_kind:     global_buffer
      - .address_space:  global
        .offset:         32
        .size:           8
        .value_kind:     global_buffer
      - .address_space:  global
        .offset:         40
        .size:           8
        .value_kind:     global_buffer
      - .actual_access:  write_only
        .address_space:  global
        .offset:         48
        .size:           8
        .value_kind:     global_buffer
      - .actual_access:  write_only
        .address_space:  global
        .offset:         56
        .size:           8
        .value_kind:     global_buffer
    .group_segment_fixed_size: 37392
    .kernarg_segment_align: 8
    .kernarg_segment_size: 64
    .language:       OpenCL C
    .language_version:
      - 2
      - 0
    .max_flat_workgroup_size: 256
    .name:           _Z9k1_kernelPKfS0_S0_PDF16_PiPfP15HIP_vector_typeIiLj2EES6_
    .private_segment_fixed_size: 0
    .sgpr_count:     32
    .sgpr_spill_count: 0
    .symbol:         _Z9k1_kernelPKfS0_S0_PDF16_PiPfP15HIP_vector_typeIiLj2EES6_.kd
    .uniform_work_group_size: 1
    .uses_dynamic_stack: false
    .vgpr_count:     120
    .vgpr_spill_count: 0
    .wavefront_size: 64
  - .agpr_count:     0
    .args:
      - .actual_access:  read_only
        .address_space:  global
        .offset:         0
        .size:           8
        .value_kind:     global_buffer
      - .actual_access:  read_only
        .address_space:  global
        .offset:         8
        .size:           8
        .value_kind:     global_buffer
      - .actual_access:  read_only
        .address_space:  global
        .offset:         16
        .size:           8
        .value_kind:     global_buffer
      - .actual_access:  read_only
        .address_space:  global
        .offset:         24
        .size:           8
        .value_kind:     global_buffer
      - .actual_access:  read_only
        .address_space:  global
        .offset:         32
        .size:           8
        .value_kind:     global_buffer
      - .actual_access:  read_only
        .address_space:  global
        .offset:         40
        .size:           8
        .value_kind:     global_buffer
      - .actual_access:  read_only
        .address_space:  global
        .offset:         48
        .size:           8
        .value_kind:     global_buffer
      - .actual_access:  read_only
        .address_space:  global
        .offset:         56
        .size:           8
        .value_kind:     global_buffer
      - .actual_access:  read_only
        .address_space:  global
        .offset:         64
        .size:           8
        .value_kind:     global_buffer
      - .actual_access:  write_only
        .address_space:  global
        .offset:         72
        .size:           8
        .value_kind:     global_buffer
      - .address_space:  global
        .offset:         80
        .size:           8
        .value_kind:     global_buffer
    .group_segment_fixed_size: 44224
    .kernarg_segment_align: 8
    .kernarg_segment_size: 88
    .language:       OpenCL C
    .language_version:
      - 2
      - 0
    .max_flat_workgroup_size: 512
    .name:           _Z11agg2_kernelPKiPKfPK15HIP_vector_typeIiLj2EEPKDF16_S2_S2_S2_S2_S2_PfS9_
    .private_segment_fixed_size: 0
    .sgpr_count:     41
    .sgpr_spill_count: 0
    .symbol:         _Z11agg2_kernelPKiPKfPK15HIP_vector_typeIiLj2EEPKDF16_S2_S2_S2_S2_S2_PfS9_.kd
    .uniform_work_group_size: 1
    .uses_dynamic_stack: false
    .vgpr_count:     80
    .vgpr_spill_count: 0
    .wavefront_size: 64
  - .agpr_count:     0
    .args:
      - .actual_access:  read_only
        .address_space:  global
        .offset:         0
        .size:           8
        .value_kind:     global_buffer
      - .actual_access:  read_only
        .address_space:  global
        .offset:         8
        .size:           8
        .value_kind:     global_buffer
      - .actual_access:  read_only
        .address_space:  global
        .offset:         16
        .size:           8
        .value_kind:     global_buffer
      - .actual_access:  read_only
        .address_space:  global
        .offset:         24
        .size:           8
        .value_kind:     global_buffer
      - .actual_access:  write_only
        .address_space:  global
        .offset:         32
        .size:           8
        .value_kind:     global_buffer
      - .offset:         40
        .size:           4
        .value_kind:     hidden_block_count_x
      - .offset:         44
        .size:           4
        .value_kind:     hidden_block_count_y
      - .offset:         48
        .size:           4
        .value_kind:     hidden_block_count_z
      - .offset:         52
        .size:           2
        .value_kind:     hidden_group_size_x
      - .offset:         54
        .size:           2
        .value_kind:     hidden_group_size_y
      - .offset:         56
        .size:           2
        .value_kind:     hidden_group_size_z
      - .offset:         58
        .size:           2
        .value_kind:     hidden_remainder_x
      - .offset:         60
        .size:           2
        .value_kind:     hidden_remainder_y
      - .offset:         62
        .size:           2
        .value_kind:     hidden_remainder_z
      - .offset:         80
        .size:           8
        .value_kind:     hidden_global_offset_x
      - .offset:         88
        .size:           8
        .value_kind:     hidden_global_offset_y
      - .offset:         96
        .size:           8
        .value_kind:     hidden_global_offset_z
      - .offset:         104
        .size:           2
        .value_kind:     hidden_grid_dims
    .group_segment_fixed_size: 512
    .kernarg_segment_align: 8
    .kernarg_segment_size: 296
    .language:       OpenCL C
    .language_version:
      - 2
      - 0
    .max_flat_workgroup_size: 256
    .name:           _Z12final_kernelPKfS0_S0_S0_Pf
    .private_segment_fixed_size: 0
    .sgpr_count:     22
    .sgpr_spill_count: 0
    .symbol:         _Z12final_kernelPKfS0_S0_S0_Pf.kd
    .uniform_work_group_size: 1
    .uses_dynamic_stack: false
    .vgpr_count:     49
    .vgpr_spill_count: 0
    .wavefront_size: 64
  - .agpr_count:     0
    .args:
      - .actual_access:  read_only
        .address_space:  global
        .offset:         0
        .size:           8
        .value_kind:     global_buffer
      - .actual_access:  read_only
        .address_space:  global
        .offset:         8
        .size:           8
        .value_kind:     global_buffer
      - .address_space:  global
        .offset:         16
        .size:           8
        .value_kind:     global_buffer
      - .address_space:  global
        .offset:         24
        .size:           8
        .value_kind:     global_buffer
      - .actual_access:  read_only
        .address_space:  global
        .offset:         32
        .size:           8
        .value_kind:     global_buffer
      - .actual_access:  read_only
        .address_space:  global
        .offset:         40
        .size:           8
        .value_kind:     global_buffer
      - .actual_access:  write_only
        .address_space:  global
        .offset:         48
        .size:           8
        .value_kind:     global_buffer
      - .address_space:  global
        .offset:         56
        .size:           8
        .value_kind:     global_buffer
    .group_segment_fixed_size: 8192
    .kernarg_segment_align: 8
    .kernarg_segment_size: 64
    .language:       OpenCL C
    .language_version:
      - 2
      - 0
    .max_flat_workgroup_size: 512
    .name:           _Z10agg_kernelILi128ELb1EEvPKiPKfP15HIP_vector_typeIiLj2EES6_PKDF16_S3_PDF16_Pf
    .private_segment_fixed_size: 0
    .sgpr_count:     66
    .sgpr_spill_count: 0
    .symbol:         _Z10agg_kernelILi128ELb1EEvPKiPKfP15HIP_vector_typeIiLj2EES6_PKDF16_S3_PDF16_Pf.kd
    .uniform_work_group_size: 1
    .uses_dynamic_stack: false
    .vgpr_count:     80
    .vgpr_spill_count: 0
    .wavefront_size: 64
